# attention-first split by unit bit 4 (the 8 value slices and both directions of a head run their mLSTM together) on top of hosted w_dn conversion
# speedup vs baseline: 1.0193x; 1.0056x over previous
; __device__ __forceinline__ int lane_id_() { int l; asm volatile("v_mbcnt_lo_u32_b32 %0, -1, 0\n\tv_mbcnt_hi_u32_b32 %0, -1, %0" : "=v"(l)); return l; }
; __global__ void __launch_bounds__(NTHREADS, 2) fwd(Args args) {
;     ...
;     if (IN(4)) {
;         const int lane = lane_id_(), tid = wave * 64 + lane; (void)tid; (void)lane;
;         const bool att_first = (vcu & 1) != 0;
;     ...
;         if (att_first) { ATT_BLOCK(); __syncthreads(); }
.LBB0_504:
	s_mov_b32 s99, 0
	v_readlane_b32 s0, v254, 34
	v_readlane_b32 s14, v254, 48
	v_readlane_b32 s1, v254, 35
	v_readlane_b32 s15, v254, 49
	s_add_u32 s0, s14, 0x4d59400
	s_addc_u32 s1, s15, 0
	v_writelane_b32 v255, s0, 16
	v_readlane_b32 s2, v254, 36
	v_readlane_b32 s3, v254, 37
	v_writelane_b32 v255, s1, 17
	s_add_u32 s0, s14, 0x14d59400
	v_writelane_b32 v255, s0, 18
	s_addc_u32 s0, s15, 0
	s_add_u32 s66, s14, 0x318e9400
	s_addc_u32 s67, s15, 0
	s_add_u32 s68, s14, 0x338e9400
	s_addc_u32 s69, s15, 0
	s_add_u32 s57, s14, 0x4de49400
	v_writelane_b32 v255, s0, 19
	s_addc_u32 s0, s15, 0
	s_cmp_lt_i32 s96, 5
	v_writelane_b32 v255, s0, 20
	s_cselect_b64 s[0:1], -1, 0
	s_cmp_gt_i32 s97, 4
	s_cselect_b64 s[2:3], -1, 0
	s_and_b64 s[0:1], s[0:1], s[2:3]
	v_writelane_b32 v255, s0, 21
	s_andn2_b64 vcc, exec, s[0:1]
	v_readlane_b32 s4, v254, 38
	v_writelane_b32 v255, s1, 22
	v_writelane_b32 v255, s76, 23
	v_writelane_b32 v255, s77, 24
	v_writelane_b32 v255, s74, 25
	v_readlane_b32 s5, v254, 39
	v_readlane_b32 s6, v254, 40
	v_readlane_b32 s7, v254, 41
	v_readlane_b32 s8, v254, 42
	v_readlane_b32 s9, v254, 43
	v_readlane_b32 s10, v254, 44
	v_readlane_b32 s11, v254, 45
	v_readlane_b32 s12, v254, 46
	v_readlane_b32 s13, v254, 47
	s_cbranch_vccnz .LBB0_659
	s_bitcmp0_b32 s74, 4
	s_cselect_b64 s[0:1], -1, 0
	v_writelane_b32 v255, s0, 26
	s_and_b64 vcc, exec, s[0:1]
	v_mbcnt_lo_u32_b32 v180, -1, 0
	v_mbcnt_hi_u32_b32 v180, -1, v180
	s_nop 0
	v_writelane_b32 v255, s1, 27
	s_cbranch_vccnz .LBB0_529
